# speedup vs baseline: 1.0246x; 1.0246x over previous
.LBB0_37:
	s_or_b64 exec, exec, s[0:1]
	v_mov_b32_e32 v98, v97
	v_mov_b32_e32 v99, v97
	v_mov_b32_e32 v5, v97
	v_mov_b32_e32 v6, v97
	v_mov_b32_e32 v7, v97
	v_mov_b32_e32 v1, v97
	v_mov_b32_e32 v2, v97
	v_mov_b32_e32 v3, v97
	s_mov_b32 s0, 0x10000
	v_or_b32_e32 v8, 0x21000, v223
	v_mfma_f32_32x32x16_f16 v[32:47], v[96:99], v[0:3], 0
	v_mfma_f32_32x32x16_f16 v[16:31], v[4:7], v[0:3], 0
	v_or_b32_e32 v114, 0x21000, v223
	v_cmp_eq_u32_e64 s[0:1], 0, v225
	s_and_b64 vcc, vcc, s[0:1]
	ds_read_b128 v[8:11], v114
	ds_read_b128 v[12:15], v114 offset:32
	ds_read_b128 v[234:237], v114 offset:64
	ds_read_b128 v[238:241], v114 offset:96
	ds_read_b128 v[242:245], v114 offset:128
	ds_read_b128 v[106:109], v114 offset:160
	ds_read_b128 v[110:113], v114 offset:192
	s_waitcnt lgkmcnt(7)
	v_mfma_f32_32x32x16_f16 v[32:47], v[180:183], v[92:95], v[32:47]
	ds_read_b128 v[0:3], v114 offset:224
	v_mfma_f32_32x32x16_f16 v[32:47], v[184:187], v[88:91], v[32:47]
	v_mfma_f32_32x32x16_f16 v[32:47], v[188:191], v[84:87], v[32:47]
	v_mfma_f32_32x32x16_f16 v[32:47], v[192:195], v[80:83], v[32:47]
	v_mfma_f32_32x32x16_f16 v[32:47], v[196:199], v[76:79], v[32:47]
	v_mfma_f32_32x32x16_f16 v[32:47], v[200:203], v[72:75], v[32:47]
	v_mfma_f32_32x32x16_f16 v[32:47], v[204:207], v[68:71], v[32:47]
	v_mfma_f32_32x32x16_f16 v[32:47], v[208:211], v[64:67], v[32:47]
	s_waitcnt lgkmcnt(0)
	v_dot2c_f32_f16_e32 v98, v92, v8
	v_mfma_f32_32x32x16_f16 v[16:31], v[148:151], v[92:95], v[16:31]
	v_dot2c_f32_f16_e32 v98, v93, v9
	v_dot2c_f32_f16_e32 v98, v94, v10
	v_dot2c_f32_f16_e32 v98, v95, v11
	v_dot2c_f32_f16_e32 v98, v88, v12
	v_mfma_f32_32x32x16_f16 v[16:31], v[152:155], v[88:91], v[16:31]
	v_dot2c_f32_f16_e32 v98, v89, v13
	v_dot2c_f32_f16_e32 v98, v90, v14
	v_dot2c_f32_f16_e32 v98, v91, v15
	v_dot2c_f32_f16_e32 v98, v84, v234
	v_mfma_f32_32x32x16_f16 v[16:31], v[156:159], v[84:87], v[16:31]
	v_dot2c_f32_f16_e32 v98, v85, v235
	v_dot2c_f32_f16_e32 v98, v86, v236
	v_dot2c_f32_f16_e32 v98, v87, v237
	v_dot2c_f32_f16_e32 v98, v80, v238
	v_mfma_f32_32x32x16_f16 v[16:31], v[160:163], v[80:83], v[16:31]
	v_dot2c_f32_f16_e32 v98, v81, v239
	v_dot2c_f32_f16_e32 v98, v82, v240
	v_dot2c_f32_f16_e32 v98, v83, v241
	v_dot2c_f32_f16_e32 v98, v76, v242
	v_mfma_f32_32x32x16_f16 v[16:31], v[164:167], v[76:79], v[16:31]
	v_dot2c_f32_f16_e32 v98, v77, v243
	v_dot2c_f32_f16_e32 v98, v78, v244
	v_dot2c_f32_f16_e32 v98, v79, v245
	v_dot2c_f32_f16_e32 v98, v72, v106
	v_mfma_f32_32x32x16_f16 v[16:31], v[168:171], v[72:75], v[16:31]
	v_dot2c_f32_f16_e32 v98, v73, v107
	v_dot2c_f32_f16_e32 v98, v74, v108
	v_dot2c_f32_f16_e32 v98, v75, v109
	v_dot2c_f32_f16_e32 v98, v68, v110
	v_mfma_f32_32x32x16_f16 v[16:31], v[172:175], v[68:71], v[16:31]
	v_dot2c_f32_f16_e32 v98, v69, v111
	v_dot2c_f32_f16_e32 v98, v70, v112
	v_dot2c_f32_f16_e32 v98, v71, v113
	v_cvt_pk_f16_f32 v7, v38, v39
	v_cvt_pk_f16_f32 v6, v36, v37
	v_cvt_pk_f16_f32 v5, v34, v35
	v_cvt_pk_f16_f32 v4, v32, v33
	v_dot2c_f32_f16_e32 v98, v64, v0
	v_dot2c_f32_f16_e32 v98, v65, v1
	v_dot2c_f32_f16_e32 v98, v66, v2
	v_mfma_f32_32x32x16_f16 v[16:31], v[176:179], v[64:67], v[16:31]
	v_dot2c_f32_f16_e32 v98, v67, v3
	v_cvt_pk_f16_f32 v35, v46, v47
	v_cvt_pk_f16_f32 v34, v44, v45
	v_cvt_pk_f16_f32 v33, v42, v43
	v_cvt_pk_f16_f32 v32, v40, v41
	ds_bpermute_b32 v36, v102, v98
	v_cvt_f32_i32_e32 v37, v226
	v_mfma_f32_32x32x16_f16 v[0:15], v[4:7], v[60:63], 0
	s_nop 3
	v_cvt_pk_f16_f32 v23, v22, v23
	v_cvt_pk_f16_f32 v22, v20, v21
	v_cvt_pk_f16_f32 v21, v18, v19
	v_cvt_pk_f16_f32 v20, v16, v17
	v_cvt_pk_f16_f32 v19, v30, v31
	v_cvt_pk_f16_f32 v18, v28, v29
	v_cvt_pk_f16_f32 v17, v26, v27
	v_mfma_f32_32x32x16_f16 v[0:15], v[32:35], v[56:59], v[0:15]
	v_cvt_pk_f16_f32 v16, v24, v25
	s_waitcnt lgkmcnt(0)
	v_add_f32_e32 v36, v98, v36
	v_cvt_f16_f32_e32 v26, v100
	v_mov_b32_e32 v98, v97
	v_lshlrev_b32_e32 v32, 4, v218
	v_mfma_f32_32x32x16_f16 v[0:15], v[20:23], v[52:55], v[0:15]
	v_fma_mixlo_f16 v20, v37, v104, v36
	v_pack_b32_f16 v20, v20, 0
	v_pack_b32_f16 v21, v26, 0
	v_cndmask_b32_e32 v96, 0, v21, vcc
	v_mfma_f32_32x32x16_f16 v[0:15], v[16:19], v[48:51], v[0:15]
	v_cndmask_b32_e32 v16, 0, v20, vcc
	v_mov_b32_e32 v17, v97
	v_mov_b32_e32 v18, v97
	v_mov_b32_e32 v19, v97
	v_cmp_ne_u32_e32 vcc, 0, v225
	s_nop 0
	v_mfma_f32_32x32x16_f16 v[0:15], v[16:19], v[96:99], v[0:15]
	v_lshlrev_b32_e32 v70, 2, v215
	v_lshl_add_u32 v70, v214, 4, v70
	global_load_dwordx4 v[16:19], v70, s[2:3]
	global_load_dwordx4 v[20:23], v70, s[2:3] offset:32
	global_load_dwordx4 v[24:27], v70, s[2:3] offset:64
	global_load_dwordx4 v[28:31], v70, s[2:3] offset:96
	s_and_saveexec_b64 s[6:7], vcc
	s_cbranch_execz .LBB0_39
	v_lshl_or_b32 v71, v251, 12, v32
	v_add_u32_e32 v71, 0x18800, v71
	s_nop 7
	ds_write_b128 v71, v[0:3]
	ds_write_b128 v71, v[4:7] offset:1024
	ds_write_b128 v71, v[8:11] offset:2048
	ds_write_b128 v71, v[12:15] offset:3072
.LBB0_39:
	s_or_b64 exec, exec, s[6:7]
	v_cvt_pk_f16_f32 v73, v118, v119
	v_cvt_pk_f16_f32 v72, v116, v117
	v_add_u32_e32 v76, v103, v105
	v_cvt_pk_f16_f32 v75, v122, v123
	v_cvt_pk_f16_f32 v74, v120, v121
	s_waitcnt lgkmcnt(0)
	s_barrier
	ds_write2_b64 v76, v[72:73], v[74:75] offset1:34
	v_cvt_pk_f16_f32 v73, v126, v127
	v_cvt_pk_f16_f32 v72, v124, v125
	v_cvt_pk_f16_f32 v75, v130, v131
	v_cvt_pk_f16_f32 v74, v128, v129
	ds_write2_b64 v76, v[72:73], v[74:75] offset0:68 offset1:102
	v_cvt_pk_f16_f32 v73, v134, v135
	v_cvt_pk_f16_f32 v72, v132, v133
	v_cvt_pk_f16_f32 v75, v138, v139
	v_cvt_pk_f16_f32 v74, v136, v137
	ds_write2_b64 v76, v[72:73], v[74:75] offset0:136 offset1:170
	v_cvt_pk_f16_f32 v73, v142, v143
	v_cvt_pk_f16_f32 v72, v140, v141
	v_cvt_pk_f16_f32 v75, v146, v147
	v_cvt_pk_f16_f32 v74, v144, v145
	ds_write2_b64 v76, v[72:73], v[74:75] offset0:204 offset1:238
	s_and_saveexec_b64 s[6:7], s[0:1]
	s_cbranch_execz .LBB0_49
	v_mov_b32_e32 v215, 0
	v_add_u32_e32 v54, v224, v223
	ds_read_b128 v[34:37], v54
	s_movk_i32 s0, 0x110
	v_mad_u32_u24 v70, v220, s0, v223
	ds_read_b128 v[38:41], v70 offset:34816
	ds_read_b128 v[42:45], v54 offset:32
	ds_read_b128 v[46:49], v70 offset:34848
	v_lshl_or_b32 v32, v251, 12, v32
	v_add_u32_e32 v78, 0x18800, v32
	v_div_scale_f32 v82, s[0:1], s10, s10, 1.0
	v_rcp_f32_e32 v84, v82
	v_div_scale_f32 v83, vcc, 1.0, s10, 1.0
	s_waitcnt vmcnt(0) lgkmcnt(2)
	v_mfma_f32_32x32x16_f16 v[16:31], v[34:37], v[38:41], v[16:31]
	ds_read_b128 v[34:37], v54 offset:64
	ds_read_b128 v[38:41], v70 offset:34880
	s_waitcnt lgkmcnt(2)
	v_mfma_f32_32x32x16_f16 v[16:31], v[42:45], v[46:49], v[16:31]
	ds_read_b128 v[42:45], v54 offset:96
	ds_read_b128 v[46:49], v70 offset:34912
	s_waitcnt lgkmcnt(2)
	v_mfma_f32_32x32x16_f16 v[16:31], v[34:37], v[38:41], v[16:31]
	ds_read_b128 v[32:35], v54 offset:128
	ds_read_b128 v[36:39], v54 offset:160
	ds_read_b128 v[50:53], v54 offset:192
	ds_read_b128 v[54:57], v54 offset:224
	ds_read_b128 v[58:61], v70 offset:34944
	ds_read_b128 v[62:65], v70 offset:34976
	ds_read_b128 v[66:69], v70 offset:35008
	ds_read_b128 v[70:73], v70 offset:35040
	s_waitcnt lgkmcnt(8)
	v_mfma_f32_32x32x16_f16 v[16:31], v[42:45], v[46:49], v[16:31]
	ds_read_b128 v[40:43], v78
	ds_read_b128 v[44:47], v78 offset:1024
	ds_read_b128 v[74:77], v78 offset:2048
	ds_read_b128 v[78:81], v78 offset:3072
	v_fma_f32 v48, -v82, v84, 1.0
	v_fmac_f32_e32 v84, v48, v84
	v_mul_f32_e32 v48, v83, v84
	s_waitcnt lgkmcnt(7)
	v_mfma_f32_32x32x16_f16 v[16:31], v[32:35], v[58:61], v[16:31]
	s_waitcnt lgkmcnt(3)
	v_add_f32_e64 v32, v0, v40
	v_add_f32_e64 v33, v1, v41
	v_add_f32_e64 v0, v42, v2
	v_add_f32_e64 v1, v43, v3
	s_waitcnt lgkmcnt(2)
	v_pk_add_f32 v[2:3], v[4:5], v[44:45]
	v_pk_add_f32 v[4:5], v[46:47], v[6:7]
	s_waitcnt lgkmcnt(1)
	v_pk_add_f32 v[6:7], v[8:9], v[74:75]
	s_waitcnt lgkmcnt(0)
	v_pk_add_f32 v[8:9], v[12:13], v[78:79]
	v_fma_f32 v12, -v82, v48, v83
	v_mfma_f32_32x32x16_f16 v[16:31], v[36:39], v[62:65], v[16:31]
	v_fmac_f32_e32 v48, v12, v84
	v_cvt_pk_f16_f32 v2, v2, v3
	v_cvt_pk_f16_f32 v3, v4, v5
	v_cvt_pk_f16_f32 v1, v0, v1
	v_cvt_pk_f16_f32 v0, v32, v33
	v_fma_f32 v4, -v82, v48, v83
	v_div_fmas_f32 v4, v4, v84, v48
	v_mfma_f32_32x32x16_f16 v[16:31], v[50:53], v[66:69], v[16:31]
	v_add_f32_e64 v40, v76, v10
	v_add_f32_e64 v41, v77, v11
	v_add_f32_e64 v10, v80, v14
	v_add_f32_e64 v11, v81, v15
	v_div_fixup_f32 v4, v4, s10, 1.0
	v_cvt_pk_f16_f32 v34, v8, v9
	v_cvt_pk_f16_f32 v32, v6, v7
	v_cvt_pk_f16_f32 v35, v10, v11
	v_cvt_pk_f16_f32 v33, v40, v41
	v_mfma_f32_32x32x16_f16 v[16:31], v[54:57], v[70:73], v[16:31]
	s_andn2_b64 vcc, exec, s[8:9]
	s_nop 10
	v_mul_f32_e32 v8, v4, v16
	v_mul_f32_e32 v9, v4, v17
	v_mul_f32_e32 v5, v4, v18
	v_mul_f32_e32 v10, v4, v19
	v_mul_f32_e32 v6, v4, v20
	v_mul_f32_e32 v11, v4, v21
	v_mul_f32_e32 v7, v4, v22
	v_mul_f32_e32 v12, v4, v23
	v_mul_f32_e32 v16, v4, v24
	v_mul_f32_e32 v20, v4, v25
	v_mul_f32_e32 v17, v4, v26
	v_mul_f32_e32 v21, v4, v27
	v_mul_f32_e32 v18, v4, v28
	v_mul_f32_e32 v22, v4, v29
	v_mul_f32_e32 v19, v4, v30
	v_mul_f32_e32 v23, v4, v31
	v_cvt_pk_f16_f32 v7, v7, v12
	v_cvt_pk_f16_f32 v6, v6, v11
	v_cvt_pk_f16_f32 v5, v5, v10
	v_cvt_pk_f16_f32 v4, v8, v9
	v_cvt_pk_f16_f32 v19, v19, v23
	v_cvt_pk_f16_f32 v18, v18, v22
	v_mfma_f32_32x32x16_f16 v[0:15], v[0:3], v[4:7], 0
	v_cvt_pk_f16_f32 v17, v17, v21
	v_cvt_pk_f16_f32 v16, v16, v20
	s_nop 1
	v_mfma_f32_32x32x16_f16 v[0:15], v[32:35], v[16:19], v[0:15]
	s_cbranch_vccnz .LBB0_48
	v_lshlrev_b32_e32 v16, 7, v220
	v_lshl_or_b32 v16, v251, 12, v16
	v_mov_b32_e32 v17, v215
	s_add_i32 s33, s33, s46
	v_lshlrev_b32_e32 v22, 2, v214
	v_lshl_add_u64 v[16:17], v[16:17], 2, s[44:45]
	v_add_u32_e32 v18, s33, v214
	s_mov_b64 s[0:1], 0
	s_movk_i32 s10, 0x3fd
	v_mov_b32_e32 v23, v215
	s_branch .LBB0_43
